# back-edge rotation (loop-back barrier becomes loop head; counter/exit test/branch and P2 streamer tail moved in front of it) in the P8 and P2 K-loops
# baseline (speedup 1.0000x reference)
.Lp2_top:
	s_barrier
	ds_read_b128 v[158:161], v217
	ds_read_b128 v[162:165], v218
	ds_read_b128 v[166:169], v219
	ds_read_b128 v[170:173], v220
	ds_read_b128 v[148:151], v221
	ds_read_b128 v[144:147], v222
	ds_read_b128 v[140:143], v223
	ds_read_b128 v[136:139], v224
	ds_read_b128 v[174:177], v233
	ds_read_b128 v[178:181], v233 offset:1024
	ds_read_b128 v[182:185], v233 offset:2048
	ds_read_b128 v[186:189], v233 offset:3072
	ds_read_b128 v[190:193], v233 offset:4096
	ds_read_b128 v[194:197], v233 offset:5120
	ds_read_b128 v[234:237], v233 offset:6144
	ds_read_b128 v[238:241], v233 offset:7168
	s_add_i32 s4, s60, s61
	s_mov_b32 s46, s94
	s_add_i32 s94, s94, 1
	s_add_i32 s5, s4, 0x200
	s_add_i32 s16, s33, s61
	s_cmpk_eq_i32 s61, 0x1e00
	s_cselect_b32 s47, s90, s5
	s_cselect_b32 s97, s91, s16
	s_add_i32 s96, s47, 0x80
	s_mov_b32 m0, s82
	s_add_i32 s5, s4, 0x100180
	buffer_load_dwordx4 v214, s[8:11], s5 offen lds
	s_add_i32 s4, s4, 0x180180
	s_mov_b32 m0, s85
	s_add_i32 vcc_lo, s97, 0x80
	buffer_load_dwordx4 v214, s[8:11], s4 offen lds
	s_lshr_b32 s4, s94, 2
	s_mul_i32 s5, s4, s34
	s_add_i32 s16, s5, s2
	s_cmp_lt_i32 s4, s3
	s_cselect_b64 s[4:5], -1, 0
	s_and_b64 s[44:45], s[4:5], exec
	s_cselect_b32 s16, s16, 0
	s_bfe_u32 s17, s94, 0x10001
	s_or_b32 s17, s17, s83
	s_bfe_u32 s67, s16, 0x50007
	s_bfe_u32 s36, s16, 0x50002
	s_and_b32 s95, s16, 3
	s_cmpk_gt_i32 s16, 0xfff
	s_cselect_b64 s[44:45], -1, 0
	v_lshl_or_b32 v156, s17, 3, v216
	s_and_b64 s[16:17], s[44:45], exec
	s_cselect_b32 s16, s25, s21
	s_cselect_b32 s17, s24, s20
	s_lshl_b32 vcc_hi, s67, 23
	s_add_u32 s17, s17, vcc_hi
	s_addc_u32 s16, s16, 0
	s_lshl_b32 vcc_hi, s36, 18
	s_add_u32 s17, s17, vcc_hi
	s_addc_u32 vcc_hi, s16, 0
	s_lshl_b32 s16, s95, 9
	s_add_u32 s16, s17, s16
	v_and_or_b32 v204, s66, 2, v200
	s_addc_u32 s17, vcc_hi, 0
	v_lshlrev_b64 v[128:129], 11, v[204:205]
	v_lshl_add_u64 v[128:129], s[16:17], 0, v[128:129]
	v_lshlrev_b32_e32 v204, 4, v156
	v_lshl_add_u64 v[132:133], v[128:129], 0, v[204:205]
	global_load_dwordx4 v[128:131], v[132:133], off nt
	s_nop 0
	global_load_dwordx4 v[132:135], v[132:133], off offset:2048 nt
	s_waitcnt vmcnt(10)
	s_waitcnt lgkmcnt(8)
	s_barrier
	s_setprio 1
	s_waitcnt lgkmcnt(7)
	v_mfma_f32_16x16x32_bf16 v[124:127], v[158:161], v[174:177], v[124:127]
	s_waitcnt lgkmcnt(6)
	v_mfma_f32_16x16x32_bf16 v[124:127], v[162:165], v[178:181], v[124:127]
	v_mfma_f32_16x16x32_bf16 v[120:123], v[166:169], v[174:177], v[120:123]
	s_nop 0
	v_mfma_f32_16x16x32_bf16 v[120:123], v[170:173], v[178:181], v[120:123]
	s_waitcnt lgkmcnt(5)
	v_mfma_f32_16x16x32_bf16 v[116:119], v[158:161], v[182:185], v[116:119]
	s_waitcnt lgkmcnt(4)
	v_mfma_f32_16x16x32_bf16 v[116:119], v[162:165], v[186:189], v[116:119]
	v_mfma_f32_16x16x32_bf16 v[112:115], v[166:169], v[182:185], v[112:115]
	s_nop 0
	v_mfma_f32_16x16x32_bf16 v[112:115], v[170:173], v[186:189], v[112:115]
	s_waitcnt lgkmcnt(3)
	v_mfma_f32_16x16x32_bf16 v[108:111], v[158:161], v[190:193], v[108:111]
	s_waitcnt lgkmcnt(2)
	v_mfma_f32_16x16x32_bf16 v[108:111], v[162:165], v[194:197], v[108:111]
	v_mfma_f32_16x16x32_bf16 v[104:107], v[166:169], v[190:193], v[104:107]
	s_nop 0
	v_mfma_f32_16x16x32_bf16 v[104:107], v[170:173], v[194:197], v[104:107]
	s_waitcnt lgkmcnt(1)
	v_mfma_f32_16x16x32_bf16 v[100:103], v[158:161], v[234:237], v[100:103]
	s_waitcnt lgkmcnt(0)
	v_mfma_f32_16x16x32_bf16 v[100:103], v[162:165], v[238:241], v[100:103]
	v_mfma_f32_16x16x32_bf16 v[96:99], v[166:169], v[234:237], v[96:99]
	s_nop 0
	v_mfma_f32_16x16x32_bf16 v[96:99], v[170:173], v[238:241], v[96:99]
	s_setprio 0
	s_setprio 1
	v_mfma_f32_16x16x32_bf16 v[92:95], v[148:151], v[174:177], v[92:95]
	s_nop 0
	v_mfma_f32_16x16x32_bf16 v[92:95], v[144:147], v[178:181], v[92:95]
	v_mfma_f32_16x16x32_bf16 v[88:91], v[140:143], v[174:177], v[88:91]
	s_nop 0
	v_mfma_f32_16x16x32_bf16 v[88:91], v[136:139], v[178:181], v[88:91]
	v_mfma_f32_16x16x32_bf16 v[84:87], v[148:151], v[182:185], v[84:87]
	s_nop 0
	v_mfma_f32_16x16x32_bf16 v[84:87], v[144:147], v[186:189], v[84:87]
	v_mfma_f32_16x16x32_bf16 v[80:83], v[140:143], v[182:185], v[80:83]
	s_nop 0
	v_mfma_f32_16x16x32_bf16 v[80:83], v[136:139], v[186:189], v[80:83]
	v_mfma_f32_16x16x32_bf16 v[76:79], v[148:151], v[190:193], v[76:79]
	s_nop 0
	v_mfma_f32_16x16x32_bf16 v[76:79], v[144:147], v[194:197], v[76:79]
	v_mfma_f32_16x16x32_bf16 v[72:75], v[140:143], v[190:193], v[72:75]
	s_nop 0
	v_mfma_f32_16x16x32_bf16 v[72:75], v[136:139], v[194:197], v[72:75]
	v_mfma_f32_16x16x32_bf16 v[68:71], v[148:151], v[234:237], v[68:71]
	s_nop 0
	v_mfma_f32_16x16x32_bf16 v[68:71], v[144:147], v[238:241], v[68:71]
	v_mfma_f32_16x16x32_bf16 v[64:67], v[140:143], v[234:237], v[64:67]
	s_nop 0
	v_mfma_f32_16x16x32_bf16 v[64:67], v[136:139], v[238:241], v[64:67]
	s_setprio 0
	s_barrier
	ds_read_b128 v[174:177], v233 offset:16384
	ds_read_b128 v[178:181], v233 offset:17408
	ds_read_b128 v[182:185], v233 offset:18432
	ds_read_b128 v[186:189], v233 offset:19456
	ds_read_b128 v[190:193], v233 offset:20480
	ds_read_b128 v[194:197], v233 offset:21504
	ds_read_b128 v[234:237], v233 offset:22528
	ds_read_b128 v[238:241], v233 offset:23552
	s_mov_b32 m0, s65
	s_add_i32 s16, s97, 0x100000
	buffer_load_dwordx4 v215, s[12:15], s97 offen lds
	s_mov_b32 m0, s68
	s_nop 0
	buffer_load_dwordx4 v215, s[12:15], s16 offen lds
	s_add_i32 s16, s97, 0x10000
	s_mov_b32 m0, s69
	s_nop 0
	buffer_load_dwordx4 v215, s[12:15], s16 offen lds
	s_add_i32 s16, s97, 0x110000
	s_mov_b32 m0, s70
	s_nop 0
	buffer_load_dwordx4 v215, s[12:15], s16 offen lds
	s_mov_b32 m0, s64
	s_add_i32 s16, s47, 0x80000
	buffer_load_dwordx4 v214, s[8:11], s47 offen lds
	s_mov_b32 m0, s71
	s_nop 0
	buffer_load_dwordx4 v214, s[8:11], s16 offen lds
	s_waitcnt vmcnt(10)
	s_waitcnt lgkmcnt(6)
	s_barrier
	s_setprio 1
	s_waitcnt lgkmcnt(7)
	v_mfma_f32_16x16x32_bf16 v[60:63], v[158:161], v[174:177], v[60:63]
	s_waitcnt lgkmcnt(6)
	v_mfma_f32_16x16x32_bf16 v[60:63], v[162:165], v[178:181], v[60:63]
	v_mfma_f32_16x16x32_bf16 v[56:59], v[166:169], v[174:177], v[56:59]
	s_nop 0
	v_mfma_f32_16x16x32_bf16 v[56:59], v[170:173], v[178:181], v[56:59]
	s_waitcnt lgkmcnt(5)
	v_mfma_f32_16x16x32_bf16 v[52:55], v[158:161], v[182:185], v[52:55]
	s_waitcnt lgkmcnt(4)
	v_mfma_f32_16x16x32_bf16 v[52:55], v[162:165], v[186:189], v[52:55]
	v_mfma_f32_16x16x32_bf16 v[48:51], v[166:169], v[182:185], v[48:51]
	s_nop 0
	v_mfma_f32_16x16x32_bf16 v[48:51], v[170:173], v[186:189], v[48:51]
	s_waitcnt lgkmcnt(3)
	v_mfma_f32_16x16x32_bf16 v[44:47], v[158:161], v[190:193], v[44:47]
	s_waitcnt lgkmcnt(2)
	v_mfma_f32_16x16x32_bf16 v[44:47], v[162:165], v[194:197], v[44:47]
	v_mfma_f32_16x16x32_bf16 v[40:43], v[166:169], v[190:193], v[40:43]
	s_nop 0
	v_mfma_f32_16x16x32_bf16 v[40:43], v[170:173], v[194:197], v[40:43]
	s_waitcnt lgkmcnt(1)
	v_mfma_f32_16x16x32_bf16 v[36:39], v[158:161], v[234:237], v[36:39]
	s_waitcnt lgkmcnt(0)
	v_mfma_f32_16x16x32_bf16 v[36:39], v[162:165], v[238:241], v[36:39]
	v_mfma_f32_16x16x32_bf16 v[32:35], v[166:169], v[234:237], v[32:35]
	s_nop 0
	v_mfma_f32_16x16x32_bf16 v[32:35], v[170:173], v[238:241], v[32:35]
	s_setprio 0
	s_setprio 1
	v_mfma_f32_16x16x32_bf16 v[28:31], v[148:151], v[174:177], v[28:31]
	s_nop 0
	v_mfma_f32_16x16x32_bf16 v[28:31], v[144:147], v[178:181], v[28:31]
	v_mfma_f32_16x16x32_bf16 v[24:27], v[140:143], v[174:177], v[24:27]
	s_nop 0
	v_mfma_f32_16x16x32_bf16 v[24:27], v[136:139], v[178:181], v[24:27]
	v_mfma_f32_16x16x32_bf16 v[20:23], v[148:151], v[182:185], v[20:23]
	s_nop 0
	v_mfma_f32_16x16x32_bf16 v[20:23], v[144:147], v[186:189], v[20:23]
	v_mfma_f32_16x16x32_bf16 v[16:19], v[140:143], v[182:185], v[16:19]
	s_nop 0
	v_mfma_f32_16x16x32_bf16 v[16:19], v[136:139], v[186:189], v[16:19]
	v_mfma_f32_16x16x32_bf16 v[12:15], v[148:151], v[190:193], v[12:15]
	s_nop 0
	v_mfma_f32_16x16x32_bf16 v[12:15], v[144:147], v[194:197], v[12:15]
	v_mfma_f32_16x16x32_bf16 v[8:11], v[140:143], v[190:193], v[8:11]
	s_nop 0
	v_mfma_f32_16x16x32_bf16 v[8:11], v[136:139], v[194:197], v[8:11]
	v_mfma_f32_16x16x32_bf16 v[4:7], v[148:151], v[234:237], v[4:7]
	s_nop 0
	v_mfma_f32_16x16x32_bf16 v[4:7], v[144:147], v[238:241], v[4:7]
	v_mfma_f32_16x16x32_bf16 v[0:3], v[140:143], v[234:237], v[0:3]
	s_nop 0
	v_mfma_f32_16x16x32_bf16 v[0:3], v[136:139], v[238:241], v[0:3]
	s_setprio 0
	s_barrier
	ds_read_b128 v[136:139], v225
	ds_read_b128 v[140:143], v226
	ds_read_b128 v[144:147], v227
	ds_read_b128 v[148:151], v228
	ds_read_b128 v[158:161], v229
	ds_read_b128 v[162:165], v230
	ds_read_b128 v[166:169], v231
	ds_read_b128 v[170:173], v232
	ds_read_b128 v[174:177], v233 offset:32768
	ds_read_b128 v[178:181], v233 offset:33792
	ds_read_b128 v[182:185], v233 offset:34816
	ds_read_b128 v[186:189], v233 offset:35840
	ds_read_b128 v[190:193], v233 offset:36864
	ds_read_b128 v[194:197], v233 offset:37888
	ds_read_b128 v[234:237], v233 offset:38912
	ds_read_b128 v[238:241], v233 offset:39936
	s_mov_b32 m0, s72
	s_add_i32 s16, s47, 0x100000
	buffer_load_dwordx4 v214, s[8:11], s16 offen lds
	s_add_i32 s16, s47, 0x180000
	s_mov_b32 m0, s73
	s_nop 0
	buffer_load_dwordx4 v214, s[8:11], s16 offen lds
	s_waitcnt vmcnt(10)
	s_waitcnt lgkmcnt(8)
	s_barrier
	s_setprio 1
	s_waitcnt lgkmcnt(7)
	v_mfma_f32_16x16x32_bf16 v[124:127], v[136:139], v[174:177], v[124:127]
	s_waitcnt lgkmcnt(6)
	v_mfma_f32_16x16x32_bf16 v[124:127], v[140:143], v[178:181], v[124:127]
	v_mfma_f32_16x16x32_bf16 v[120:123], v[144:147], v[174:177], v[120:123]
	s_nop 0
	v_mfma_f32_16x16x32_bf16 v[120:123], v[148:151], v[178:181], v[120:123]
	s_waitcnt lgkmcnt(5)
	v_mfma_f32_16x16x32_bf16 v[116:119], v[136:139], v[182:185], v[116:119]
	s_waitcnt lgkmcnt(4)
	v_mfma_f32_16x16x32_bf16 v[116:119], v[140:143], v[186:189], v[116:119]
	v_mfma_f32_16x16x32_bf16 v[112:115], v[144:147], v[182:185], v[112:115]
	s_nop 0
	v_mfma_f32_16x16x32_bf16 v[112:115], v[148:151], v[186:189], v[112:115]
	s_waitcnt lgkmcnt(3)
	v_mfma_f32_16x16x32_bf16 v[108:111], v[136:139], v[190:193], v[108:111]
	s_waitcnt lgkmcnt(2)
	v_mfma_f32_16x16x32_bf16 v[108:111], v[140:143], v[194:197], v[108:111]
	v_mfma_f32_16x16x32_bf16 v[104:107], v[144:147], v[190:193], v[104:107]
	s_nop 0
	v_mfma_f32_16x16x32_bf16 v[104:107], v[148:151], v[194:197], v[104:107]
	s_waitcnt lgkmcnt(1)
	v_mfma_f32_16x16x32_bf16 v[100:103], v[136:139], v[234:237], v[100:103]
	s_waitcnt lgkmcnt(0)
	v_mfma_f32_16x16x32_bf16 v[100:103], v[140:143], v[238:241], v[100:103]
	v_mfma_f32_16x16x32_bf16 v[96:99], v[144:147], v[234:237], v[96:99]
	s_nop 0
	v_mfma_f32_16x16x32_bf16 v[96:99], v[148:151], v[238:241], v[96:99]
	s_setprio 0
	s_setprio 1
	v_mfma_f32_16x16x32_bf16 v[92:95], v[158:161], v[174:177], v[92:95]
	s_nop 0
	v_mfma_f32_16x16x32_bf16 v[92:95], v[162:165], v[178:181], v[92:95]
	v_mfma_f32_16x16x32_bf16 v[88:91], v[166:169], v[174:177], v[88:91]
	s_nop 0
	v_mfma_f32_16x16x32_bf16 v[88:91], v[170:173], v[178:181], v[88:91]
	v_mfma_f32_16x16x32_bf16 v[84:87], v[158:161], v[182:185], v[84:87]
	s_nop 0
	v_mfma_f32_16x16x32_bf16 v[84:87], v[162:165], v[186:189], v[84:87]
	v_mfma_f32_16x16x32_bf16 v[80:83], v[166:169], v[182:185], v[80:83]
	s_nop 0
	v_mfma_f32_16x16x32_bf16 v[80:83], v[170:173], v[186:189], v[80:83]
	v_mfma_f32_16x16x32_bf16 v[76:79], v[158:161], v[190:193], v[76:79]
	s_nop 0
	v_mfma_f32_16x16x32_bf16 v[76:79], v[162:165], v[194:197], v[76:79]
	v_mfma_f32_16x16x32_bf16 v[72:75], v[166:169], v[190:193], v[72:75]
	s_nop 0
	v_mfma_f32_16x16x32_bf16 v[72:75], v[170:173], v[194:197], v[72:75]
	v_mfma_f32_16x16x32_bf16 v[68:71], v[158:161], v[234:237], v[68:71]
	s_nop 0
	v_mfma_f32_16x16x32_bf16 v[68:71], v[162:165], v[238:241], v[68:71]
	v_mfma_f32_16x16x32_bf16 v[64:67], v[166:169], v[234:237], v[64:67]
	s_nop 0
	v_mfma_f32_16x16x32_bf16 v[64:67], v[170:173], v[238:241], v[64:67]
	s_setprio 0
	s_barrier
	ds_read_b128 v[174:177], v233 offset:49152
	ds_read_b128 v[178:181], v233 offset:50176
	ds_read_b128 v[182:185], v233 offset:51200
	ds_read_b128 v[186:189], v233 offset:52224
	ds_read_b128 v[190:193], v233 offset:53248
	ds_read_b128 v[194:197], v233 offset:54272
	ds_read_b128 v[234:237], v233 offset:55296
	ds_read_b128 v[238:241], v233 offset:56320
	s_mov_b32 m0, s76
	s_add_i32 s16, s97, 0x100080
	buffer_load_dwordx4 v215, s[12:15], vcc_lo offen lds
	s_mov_b32 m0, s77
	s_add_i32 s47, s47, 0x80080
	buffer_load_dwordx4 v215, s[12:15], s16 offen lds
	s_add_i32 s16, s97, 0x10080
	s_mov_b32 m0, s80
	s_add_i32 s97, s97, 0x110080
	buffer_load_dwordx4 v215, s[12:15], s16 offen lds
	s_mov_b32 m0, s81
	s_nop 0
	buffer_load_dwordx4 v215, s[12:15], s97 offen lds
	s_mov_b32 m0, s78
	s_nop 0
	buffer_load_dwordx4 v214, s[8:11], s96 offen lds
	s_mov_b32 m0, s79
	s_nop 0
	buffer_load_dwordx4 v214, s[8:11], s47 offen lds
	s_bitcmp0_b32 s46, 0
	s_mov_b32 s98, 0xffff
	s_cselect_b32 s98, 0xffff0000, s98
	s_waitcnt vmcnt(8)
	s_waitcnt lgkmcnt(6)
	s_barrier
	s_setprio 1
	s_waitcnt lgkmcnt(7)
	v_mfma_f32_16x16x32_bf16 v[60:63], v[136:139], v[174:177], v[60:63]
	s_waitcnt lgkmcnt(6)
	v_mfma_f32_16x16x32_bf16 v[60:63], v[140:143], v[178:181], v[60:63]
	v_mfma_f32_16x16x32_bf16 v[56:59], v[144:147], v[174:177], v[56:59]
	v_mul_f32_e32 v128, 0x42800000, v128
	v_mfma_f32_16x16x32_bf16 v[56:59], v[148:151], v[178:181], v[56:59]
	v_mul_f32_e32 v130, 0x42800000, v130
	s_waitcnt lgkmcnt(5)
	v_mfma_f32_16x16x32_bf16 v[52:55], v[136:139], v[182:185], v[52:55]
	s_waitcnt lgkmcnt(4)
	v_mfma_f32_16x16x32_bf16 v[52:55], v[140:143], v[186:189], v[52:55]
	v_mfma_f32_16x16x32_bf16 v[48:51], v[144:147], v[182:185], v[48:51]
	v_mul_f32_e32 v132, 0x42800000, v132
	v_mfma_f32_16x16x32_bf16 v[48:51], v[148:151], v[186:189], v[48:51]
	v_mul_f32_e32 v134, 0x42800000, v134
	s_waitcnt lgkmcnt(3)
	v_mfma_f32_16x16x32_bf16 v[44:47], v[136:139], v[190:193], v[44:47]
	s_waitcnt lgkmcnt(2)
	v_mfma_f32_16x16x32_bf16 v[44:47], v[140:143], v[194:197], v[44:47]
	v_mfma_f32_16x16x32_bf16 v[40:43], v[144:147], v[190:193], v[40:43]
	v_mul_f32_e32 v129, 0x42800000, v129
	v_mfma_f32_16x16x32_bf16 v[40:43], v[148:151], v[194:197], v[40:43]
	v_mul_f32_e32 v131, 0x42800000, v131
	s_waitcnt lgkmcnt(1)
	v_mfma_f32_16x16x32_bf16 v[36:39], v[136:139], v[234:237], v[36:39]
	s_waitcnt lgkmcnt(0)
	v_mfma_f32_16x16x32_bf16 v[36:39], v[140:143], v[238:241], v[36:39]
	v_mfma_f32_16x16x32_bf16 v[32:35], v[144:147], v[234:237], v[32:35]
	v_mul_f32_e32 v133, 0x42800000, v133
	v_mfma_f32_16x16x32_bf16 v[32:35], v[148:151], v[238:241], v[32:35]
	v_mul_f32_e32 v135, 0x42800000, v135
	s_setprio 0
	s_setprio 1
	v_mfma_f32_16x16x32_bf16 v[28:31], v[158:161], v[174:177], v[28:31]
	v_cvt_pk_fp8_f32 v204, v128, v132
	v_mfma_f32_16x16x32_bf16 v[28:31], v[162:165], v[178:181], v[28:31]
	v_mfma_f32_16x16x32_bf16 v[24:27], v[166:169], v[174:177], v[24:27]
	v_cvt_pk_fp8_f32 v204, v128, v132 op_sel:[0,0,1]
	v_mfma_f32_16x16x32_bf16 v[24:27], v[170:173], v[178:181], v[24:27]
	v_mfma_f32_16x16x32_bf16 v[20:23], v[158:161], v[182:185], v[20:23]
	v_cvt_pk_fp8_f32 v250, v129, v133
	v_mfma_f32_16x16x32_bf16 v[20:23], v[162:165], v[186:189], v[20:23]
	v_mfma_f32_16x16x32_bf16 v[16:19], v[166:169], v[182:185], v[16:19]
	v_cvt_pk_fp8_f32 v250, v129, v133 op_sel:[0,0,1]
	v_mfma_f32_16x16x32_bf16 v[16:19], v[170:173], v[186:189], v[16:19]
	v_mfma_f32_16x16x32_bf16 v[12:15], v[158:161], v[190:193], v[12:15]
	v_cvt_pk_fp8_f32 v251, v130, v134
	v_mfma_f32_16x16x32_bf16 v[12:15], v[162:165], v[194:197], v[12:15]
	v_bfi_b32 v152, s98, v204, v152
	v_mfma_f32_16x16x32_bf16 v[8:11], v[166:169], v[190:193], v[8:11]
	v_cvt_pk_fp8_f32 v251, v130, v134 op_sel:[0,0,1]
	v_mfma_f32_16x16x32_bf16 v[8:11], v[170:173], v[194:197], v[8:11]
	v_bfi_b32 v153, s98, v250, v153
	v_mfma_f32_16x16x32_bf16 v[4:7], v[158:161], v[234:237], v[4:7]
	v_cvt_pk_fp8_f32 v252, v131, v135
	v_mfma_f32_16x16x32_bf16 v[4:7], v[162:165], v[238:241], v[4:7]
	v_bfi_b32 v154, s98, v251, v154
	v_mfma_f32_16x16x32_bf16 v[0:3], v[166:169], v[234:237], v[0:3]
	v_cvt_pk_fp8_f32 v252, v131, v135 op_sel:[0,0,1]
	v_mfma_f32_16x16x32_bf16 v[0:3], v[170:173], v[238:241], v[0:3]
	v_bfi_b32 v155, s98, v252, v155
	s_setprio 0
	s_bitcmp0_b32 s46, 0
	s_mov_b64 s[46:47], -1
	s_cbranch_scc0 .LBB0_345
	s_andn2_b64 vcc, exec, s[4:5]
	s_cbranch_vccnz .LBB0_345
	s_lshl_b32 s4, s67, 10
	s_lshl_b32 s5, s95, 8
	s_or_b32 s16, s4, s5
	s_and_b64 s[4:5], s[44:45], exec
	s_cselect_b32 s4, 8, 0
	v_lshlrev_b32_e32 v128, 3, v156
	s_or_b32 s4, s4, s16
	v_and_b32_e32 v128, 0xf0, v128
	v_or_b32_e32 v128, s4, v128
	v_or_b32_e32 v204, v128, v202
	v_lshlrev_b64 v[128:129], 12, v[204:205]
	v_lshl_add_u64 v[128:129], s[6:7], 0, v[128:129]
	s_lshl_b32 s36, s36, 7
	v_lshl_add_u64 v[128:129], v[128:129], 0, s[36:37]
	v_lshl_add_u64 v[128:129], v[128:129], 0, v[200:201]
	v_add_co_u32_e32 v130, vcc, 0x1000, v128
	global_store_dword v[128:129], v152, off
	s_nop 0
	v_addc_co_u32_e32 v131, vcc, 0, v129, vcc
	global_store_dword v[130:131], v153, off
	v_add_co_u32_e32 v130, vcc, 0x2000, v128
	s_nop 1
	v_addc_co_u32_e32 v131, vcc, 0, v129, vcc
	v_add_co_u32_e32 v128, vcc, 0x3000, v128
	global_store_dword v[130:131], v154, off
	s_nop 0
	v_addc_co_u32_e32 v129, vcc, 0, v129, vcc
	global_store_dword v[128:129], v155, off
	s_branch .LBB0_345
.LBB0_345:
.LBB0_346:
	s_addk_i32 s61, 0x100
	s_add_i32 s66, s66, 2
	s_cmpk_eq_i32 s61, 0x1f00
	s_cbranch_scc1 .Lp2_exit
	s_branch .Lp2_top
.Lp2_exit:
	s_barrier
	v_mov_b32_e32 v204, v152
	v_mov_b32_e32 v234, v153
	v_mov_b32_e32 v235, v154
	v_mov_b32_e32 v236, v155

.LBB0_1228:
	s_add_i32 s28, s61, 0x180
	s_add_i32 s29, s60, 0x180
	s_waitcnt lgkmcnt(0)
	s_barrier
	s_setprio 1
	v_mfma_scale_f32_16x16x128_f8f6f4 v[128:131], v[24:31], v[56:63], 0, v201, v201 op_sel_hi:[0,0,0]
	v_mfma_scale_f32_16x16x128_f8f6f4 v[124:127], v[16:23], v[56:63], 0, v201, v201 op_sel_hi:[0,0,0]
	v_mfma_scale_f32_16x16x128_f8f6f4 v[120:123], v[24:31], v[48:55], 0, v201, v201 op_sel_hi:[0,0,0]
	v_mfma_scale_f32_16x16x128_f8f6f4 v[116:119], v[16:23], v[48:55], 0, v201, v201 op_sel_hi:[0,0,0]
	v_mfma_scale_f32_16x16x128_f8f6f4 v[112:115], v[24:31], v[40:47], 0, v201, v201 op_sel_hi:[0,0,0]
	v_mfma_scale_f32_16x16x128_f8f6f4 v[108:111], v[16:23], v[40:47], 0, v201, v201 op_sel_hi:[0,0,0]
	v_mfma_scale_f32_16x16x128_f8f6f4 v[104:107], v[24:31], v[32:39], 0, v201, v201 op_sel_hi:[0,0,0]
	v_mfma_scale_f32_16x16x128_f8f6f4 v[100:103], v[16:23], v[32:39], 0, v201, v201 op_sel_hi:[0,0,0]
	s_setprio 0
	s_setprio 1
	v_mfma_scale_f32_16x16x128_f8f6f4 v[96:99], v[8:15], v[56:63], 0, v201, v201 op_sel_hi:[0,0,0]
	v_mfma_scale_f32_16x16x128_f8f6f4 v[92:95], v[0:7], v[56:63], 0, v201, v201 op_sel_hi:[0,0,0]
	v_mfma_scale_f32_16x16x128_f8f6f4 v[88:91], v[8:15], v[48:55], 0, v201, v201 op_sel_hi:[0,0,0]
	v_mfma_scale_f32_16x16x128_f8f6f4 v[84:87], v[0:7], v[48:55], 0, v201, v201 op_sel_hi:[0,0,0]
	v_mfma_scale_f32_16x16x128_f8f6f4 v[80:83], v[8:15], v[40:47], 0, v201, v201 op_sel_hi:[0,0,0]
	v_mfma_scale_f32_16x16x128_f8f6f4 v[76:79], v[0:7], v[40:47], 0, v201, v201 op_sel_hi:[0,0,0]
	v_mfma_scale_f32_16x16x128_f8f6f4 v[72:75], v[8:15], v[32:39], 0, v201, v201 op_sel_hi:[0,0,0]
	v_mfma_scale_f32_16x16x128_f8f6f4 v[68:71], v[0:7], v[32:39], 0, v201, v201 op_sel_hi:[0,0,0]
	s_setprio 0
	s_barrier
	ds_read_b128 v[24:27], v205 offset:0x8000
	ds_read_b128 v[28:31], v205 offset:0x8400
	ds_read_b128 v[16:19], v205 offset:0x8800
	ds_read_b128 v[20:23], v205 offset:0x8c00
	ds_read_b128 v[32:35], v204 offset:0x8000
	ds_read_b128 v[36:39], v204 offset:0x8400
	ds_read_b128 v[40:43], v204 offset:0x8800
	ds_read_b128 v[44:47], v204 offset:0x8c00
	ds_read_b128 v[48:51], v204 offset:0x9000
	ds_read_b128 v[52:55], v204 offset:0x9400
	ds_read_b128 v[56:59], v204 offset:0x9800
	ds_read_b128 v[60:63], v204 offset:0x9c00
	ds_read_b128 v[8:11], v205 offset:0xc000
	ds_read_b128 v[12:15], v205 offset:0xc400
	ds_read_b128 v[0:3], v205 offset:0xc800
	ds_read_b128 v[4:7], v205 offset:0xcc00
	s_mov_b32 m0, s44
	s_nop 0
	buffer_load_dwordx4 v216, s[4:7], s33 offen lds
	s_mov_b32 m0, s45
	s_nop 0
	buffer_load_dwordx4 v215, s[4:7], s33 offen lds
	s_waitcnt vmcnt(8)
	s_waitcnt lgkmcnt(4)
	s_barrier
	s_setprio 1
	v_mfma_scale_f32_16x16x128_f8f6f4 v[192:195], v[24:31], v[32:39], v[192:195], v201, v201 op_sel_hi:[0,0,0]
	v_mfma_scale_f32_16x16x128_f8f6f4 v[188:191], v[16:23], v[32:39], v[188:191], v201, v201 op_sel_hi:[0,0,0]
	v_mfma_scale_f32_16x16x128_f8f6f4 v[184:187], v[24:31], v[40:47], v[184:187], v201, v201 op_sel_hi:[0,0,0]
	v_mfma_scale_f32_16x16x128_f8f6f4 v[180:183], v[16:23], v[40:47], v[180:183], v201, v201 op_sel_hi:[0,0,0]
	v_mfma_scale_f32_16x16x128_f8f6f4 v[176:179], v[24:31], v[48:55], v[176:179], v201, v201 op_sel_hi:[0,0,0]
	v_mfma_scale_f32_16x16x128_f8f6f4 v[172:175], v[16:23], v[48:55], v[172:175], v201, v201 op_sel_hi:[0,0,0]
	v_mfma_scale_f32_16x16x128_f8f6f4 v[168:171], v[24:31], v[56:63], v[168:171], v201, v201 op_sel_hi:[0,0,0]
	v_mfma_scale_f32_16x16x128_f8f6f4 v[164:167], v[16:23], v[56:63], v[164:167], v201, v201 op_sel_hi:[0,0,0]
	s_setprio 0
	s_setprio 1
	s_waitcnt lgkmcnt(2)
	v_mfma_scale_f32_16x16x128_f8f6f4 v[160:163], v[8:15], v[32:39], v[160:163], v201, v201 op_sel_hi:[0,0,0]
	s_waitcnt lgkmcnt(0)
	v_mfma_scale_f32_16x16x128_f8f6f4 v[156:159], v[0:7], v[32:39], v[156:159], v201, v201 op_sel_hi:[0,0,0]
	v_mfma_scale_f32_16x16x128_f8f6f4 v[152:155], v[8:15], v[40:47], v[152:155], v201, v201 op_sel_hi:[0,0,0]
	v_mfma_scale_f32_16x16x128_f8f6f4 v[148:151], v[0:7], v[40:47], v[148:151], v201, v201 op_sel_hi:[0,0,0]
	v_mfma_scale_f32_16x16x128_f8f6f4 v[144:147], v[8:15], v[48:55], v[144:147], v201, v201 op_sel_hi:[0,0,0]
	v_mfma_scale_f32_16x16x128_f8f6f4 v[140:143], v[0:7], v[48:55], v[140:143], v201, v201 op_sel_hi:[0,0,0]
	v_mfma_scale_f32_16x16x128_f8f6f4 v[136:139], v[8:15], v[56:63], v[136:139], v201, v201 op_sel_hi:[0,0,0]
	v_mfma_scale_f32_16x16x128_f8f6f4 v[132:135], v[0:7], v[56:63], v[132:135], v201, v201 op_sel_hi:[0,0,0]
	s_setprio 0
	s_barrier
	ds_read_b128 v[32:35], v204 offset:0xc000
	ds_read_b128 v[36:39], v204 offset:0xc400
	ds_read_b128 v[40:43], v204 offset:0xc800
	ds_read_b128 v[44:47], v204 offset:0xcc00
	ds_read_b128 v[48:51], v204 offset:0xd000
	ds_read_b128 v[52:55], v204 offset:0xd400
	ds_read_b128 v[56:59], v204 offset:0xd800
	ds_read_b128 v[60:63], v204 offset:0xdc00
	s_mov_b32 m0, s48
	s_mov_b32 s10, s6
	s_mov_b32 s11, s7
	buffer_load_dwordx4 v203, s[8:11], s29 offen lds
	s_add_i32 s29, s60, 0x80180
	s_mov_b32 m0, s49
	s_nop 0
	buffer_load_dwordx4 v203, s[8:11], s29 offen lds
	s_add_i32 s29, s60, 0x8180
	s_mov_b32 m0, s62
	s_nop 0
	buffer_load_dwordx4 v203, s[8:11], s29 offen lds
	s_add_i32 s29, s60, 0x88180
	s_mov_b32 m0, s63
	s_nop 0
	buffer_load_dwordx4 v203, s[8:11], s29 offen lds
	s_mov_b32 m0, s50
	s_nop 0
	buffer_load_dwordx4 v214, s[4:7], s28 offen lds
	s_mov_b32 m0, s51
	s_nop 0
	buffer_load_dwordx4 v217, s[4:7], s28 offen lds
	s_waitcnt vmcnt(8)
	s_waitcnt lgkmcnt(0)
	s_barrier
	s_setprio 1
	v_mfma_scale_f32_16x16x128_f8f6f4 v[128:131], v[24:31], v[32:39], v[128:131], v201, v201 op_sel_hi:[0,0,0]
	v_mfma_scale_f32_16x16x128_f8f6f4 v[124:127], v[16:23], v[32:39], v[124:127], v201, v201 op_sel_hi:[0,0,0]
	v_mfma_scale_f32_16x16x128_f8f6f4 v[120:123], v[24:31], v[40:47], v[120:123], v201, v201 op_sel_hi:[0,0,0]
	v_mfma_scale_f32_16x16x128_f8f6f4 v[116:119], v[16:23], v[40:47], v[116:119], v201, v201 op_sel_hi:[0,0,0]
	v_mfma_scale_f32_16x16x128_f8f6f4 v[112:115], v[24:31], v[48:55], v[112:115], v201, v201 op_sel_hi:[0,0,0]
	v_mfma_scale_f32_16x16x128_f8f6f4 v[108:111], v[16:23], v[48:55], v[108:111], v201, v201 op_sel_hi:[0,0,0]
	v_mfma_scale_f32_16x16x128_f8f6f4 v[104:107], v[24:31], v[56:63], v[104:107], v201, v201 op_sel_hi:[0,0,0]
	v_mfma_scale_f32_16x16x128_f8f6f4 v[100:103], v[16:23], v[56:63], v[100:103], v201, v201 op_sel_hi:[0,0,0]
	s_setprio 0
	s_setprio 1
	v_mfma_scale_f32_16x16x128_f8f6f4 v[96:99], v[8:15], v[32:39], v[96:99], v201, v201 op_sel_hi:[0,0,0]
	v_mfma_scale_f32_16x16x128_f8f6f4 v[92:95], v[0:7], v[32:39], v[92:95], v201, v201 op_sel_hi:[0,0,0]
	v_mfma_scale_f32_16x16x128_f8f6f4 v[88:91], v[8:15], v[40:47], v[88:91], v201, v201 op_sel_hi:[0,0,0]
	v_mfma_scale_f32_16x16x128_f8f6f4 v[84:87], v[0:7], v[40:47], v[84:87], v201, v201 op_sel_hi:[0,0,0]
	v_mfma_scale_f32_16x16x128_f8f6f4 v[80:83], v[8:15], v[48:55], v[80:83], v201, v201 op_sel_hi:[0,0,0]
	v_mfma_scale_f32_16x16x128_f8f6f4 v[76:79], v[0:7], v[48:55], v[76:79], v201, v201 op_sel_hi:[0,0,0]
	v_mfma_scale_f32_16x16x128_f8f6f4 v[72:75], v[8:15], v[56:63], v[72:75], v201, v201 op_sel_hi:[0,0,0]
	v_mfma_scale_f32_16x16x128_f8f6f4 v[68:71], v[0:7], v[56:63], v[68:71], v201, v201 op_sel_hi:[0,0,0]
	s_setprio 0
	s_barrier
	s_waitcnt vmcnt(16)
	v_mbcnt_lo_u32_b32 v0, -1, 0
	v_mbcnt_hi_u32_b32 v0, -1, v0
	s_add_i32 s29, s60, 0x200
	v_lshl_add_u32 v0, v0, 4, s37
	v_ashrrev_i32_e32 v1, 31, v0
	v_lshrrev_b32_e32 v1, 22, v1
	v_add_u32_e32 v1, v0, v1
	v_ashrrev_i32_e32 v1, 10, v1
	v_mul_i32_i24_e32 v2, 0x400, v1
	v_sub_u32_e32 v2, v0, v2
	v_lshrrev_b32_e32 v3, 4, v2
	v_bitop3_b32 v3, v3, v2, 32 bitop3:0x6c
	v_ashrrev_i32_e32 v2, 31, v2
	v_lshrrev_b32_e32 v2, 26, v2
	v_add_u32_e32 v2, v3, v2
	v_and_b32_e32 v2, 0xc0, v2
	v_add_u32_e32 v0, 0x2000, v0
	v_sub_u32_e32 v2, v3, v2
	v_ashrrev_i32_e32 v3, 31, v0
	v_lshrrev_b32_e32 v3, 22, v3
	v_add_u32_e32 v3, v0, v3
	v_ashrrev_i32_e32 v3, 10, v3
	v_mul_i32_i24_e32 v4, 0x400, v3
	v_sub_u32_e32 v0, v0, v4
	v_lshrrev_b32_e32 v4, 4, v0
	v_bitop3_b32 v4, v4, v0, 32 bitop3:0x6c
	v_ashrrev_i32_e32 v0, 31, v0
	v_lshrrev_b32_e32 v0, 26, v0
	v_add_u32_e32 v0, v4, v0
	v_and_b32_e32 v0, 0xffc0, v0
	v_sub_u32_e32 v0, v4, v0
	v_lshrrev_b16_e32 v4, 7, v0
	v_and_b32_e32 v4, 1, v4
	v_add_u16_e32 v0, v0, v4
	v_lshlrev_b32_e32 v1, 5, v1
	v_ashrrev_i16_sdwa v2, v202, sext(v2) dst_sel:DWORD dst_unused:UNUSED_PAD src0_sel:DWORD src1_sel:BYTE_0
	v_lshlrev_b32_e32 v3, 5, v3
	v_ashrrev_i16_sdwa v0, v202, sext(v0) dst_sel:DWORD dst_unused:UNUSED_PAD src0_sel:DWORD src1_sel:BYTE_0
	v_and_b32_e32 v1, 32, v1
	v_bfe_i32 v2, v2, 0, 16
	v_and_b32_e32 v3, 32, v3
	v_bfe_i32 v0, v0, 0, 16
	v_add_lshl_u32 v1, v1, v2, 1
	v_add_lshl_u32 v0, v3, v0, 1
	v_lshl_add_u32 v32, v231, 12, v1
	v_lshl_add_u32 v33, v228, 12, v0
	v_lshl_add_u32 v34, v229, 12, v1
	v_lshl_add_u32 v35, v230, 12, v0
	s_mov_b32 s33, 0
	s_add_i32 s66, s28, 0x80
	s_cmp_eq_u32 s33, 28
	s_cselect_b64 vcc, -1, 0
.LBB0_1229:
	s_barrier
	ds_read_b128 v[16:19], v205 offset:0
	ds_read_b128 v[20:23], v205 offset:0x400
	ds_read_b128 v[24:27], v205 offset:0x800
	ds_read_b128 v[28:31], v205 offset:0xc00
	ds_read_b128 v[36:39], v204 offset:0
	ds_read_b128 v[40:43], v204 offset:0x400
	ds_read_b128 v[44:47], v204 offset:0x800
	ds_read_b128 v[48:51], v204 offset:0xc00
	ds_read_b128 v[52:55], v204 offset:0x1000
	ds_read_b128 v[56:59], v204 offset:0x1400
	ds_read_b128 v[228:231], v204 offset:0x1800
	ds_read_b128 v[232:235], v204 offset:0x1c00
	ds_read_b128 v[8:11], v205 offset:0x4000
	ds_read_b128 v[12:15], v205 offset:0x4400
	ds_read_b128 v[0:3], v205 offset:0x4800
	ds_read_b128 v[4:7], v205 offset:0x4c00
	s_and_b64 s[60:61], vcc, exec
	s_cselect_b32 s66, s72, s66
	s_cselect_b32 s61, s73, s29
	s_add_i32 s60, s66, 0x80
	s_mov_b32 m0, s65
	s_nop 0
	buffer_load_dwordx4 v216, s[4:7], s28 offen lds
	s_mov_b32 m0, s68
	s_nop 0
	buffer_load_dwordx4 v215, s[4:7], s28 offen lds
	s_waitcnt vmcnt(8)
	s_waitcnt lgkmcnt(4)
	s_barrier
	s_setprio 1
	v_mfma_scale_f32_16x16x128_f8f6f4 v[192:195], v[16:23], v[36:43], v[192:195], v201, v201 op_sel_hi:[0,0,0]
	v_mfma_scale_f32_16x16x128_f8f6f4 v[188:191], v[24:31], v[36:43], v[188:191], v201, v201 op_sel_hi:[0,0,0]
	v_mfma_scale_f32_16x16x128_f8f6f4 v[184:187], v[16:23], v[44:51], v[184:187], v201, v201 op_sel_hi:[0,0,0]
	v_mfma_scale_f32_16x16x128_f8f6f4 v[180:183], v[24:31], v[44:51], v[180:183], v201, v201 op_sel_hi:[0,0,0]
	v_mfma_scale_f32_16x16x128_f8f6f4 v[176:179], v[16:23], v[52:59], v[176:179], v201, v201 op_sel_hi:[0,0,0]
	v_mfma_scale_f32_16x16x128_f8f6f4 v[172:175], v[24:31], v[52:59], v[172:175], v201, v201 op_sel_hi:[0,0,0]
	v_mfma_scale_f32_16x16x128_f8f6f4 v[168:171], v[16:23], v[228:235], v[168:171], v201, v201 op_sel_hi:[0,0,0]
	v_mfma_scale_f32_16x16x128_f8f6f4 v[164:167], v[24:31], v[228:235], v[164:167], v201, v201 op_sel_hi:[0,0,0]
	s_setprio 0
	s_setprio 1
	s_waitcnt lgkmcnt(2)
	v_mfma_scale_f32_16x16x128_f8f6f4 v[160:163], v[8:15], v[36:43], v[160:163], v201, v201 op_sel_hi:[0,0,0]
	s_waitcnt lgkmcnt(0)
	v_mfma_scale_f32_16x16x128_f8f6f4 v[156:159], v[0:7], v[36:43], v[156:159], v201, v201 op_sel_hi:[0,0,0]
	v_mfma_scale_f32_16x16x128_f8f6f4 v[152:155], v[8:15], v[44:51], v[152:155], v201, v201 op_sel_hi:[0,0,0]
	v_mfma_scale_f32_16x16x128_f8f6f4 v[148:151], v[0:7], v[44:51], v[148:151], v201, v201 op_sel_hi:[0,0,0]
	v_mfma_scale_f32_16x16x128_f8f6f4 v[144:147], v[8:15], v[52:59], v[144:147], v201, v201 op_sel_hi:[0,0,0]
	v_mfma_scale_f32_16x16x128_f8f6f4 v[140:143], v[0:7], v[52:59], v[140:143], v201, v201 op_sel_hi:[0,0,0]
	v_mfma_scale_f32_16x16x128_f8f6f4 v[136:139], v[8:15], v[228:235], v[136:139], v201, v201 op_sel_hi:[0,0,0]
	v_mfma_scale_f32_16x16x128_f8f6f4 v[132:135], v[0:7], v[228:235], v[132:135], v201, v201 op_sel_hi:[0,0,0]
	s_setprio 0
	s_barrier
	ds_read_b128 v[36:39], v204 offset:0x4000
	ds_read_b128 v[40:43], v204 offset:0x4400
	ds_read_b128 v[44:47], v204 offset:0x4800
	ds_read_b128 v[48:51], v204 offset:0x4c00
	ds_read_b128 v[52:55], v204 offset:0x5000
	ds_read_b128 v[56:59], v204 offset:0x5400
	ds_read_b128 v[228:231], v204 offset:0x5800
	ds_read_b128 v[232:235], v204 offset:0x5c00
	s_mov_b32 m0, s39
	s_nop 0
	buffer_load_dwordx4 v203, s[8:11], s61 offen lds
	s_add_i32 s67, s61, 0x80000
	s_mov_b32 m0, s40
	v_cndmask_b32_e32 v60, v214, v32, vcc
	buffer_load_dwordx4 v203, s[8:11], s67 offen lds
	s_add_i32 s67, s61, 0x8000
	s_mov_b32 m0, s41
	v_cndmask_b32_e32 v61, v217, v33, vcc
	buffer_load_dwordx4 v203, s[8:11], s67 offen lds
	s_add_i32 s67, s61, 0x88000
	s_mov_b32 m0, s42
	s_nop 0
	buffer_load_dwordx4 v203, s[8:11], s67 offen lds
	s_mov_b32 m0, s38
	s_nop 0
	buffer_load_dwordx4 v60, s[4:7], s66 offen lds
	s_mov_b32 m0, s43
	s_nop 0
	buffer_load_dwordx4 v61, s[4:7], s66 offen lds
	s_waitcnt vmcnt(8)
	s_waitcnt lgkmcnt(0)
	s_barrier
	s_setprio 1
	v_mfma_scale_f32_16x16x128_f8f6f4 v[128:131], v[16:23], v[36:43], v[128:131], v201, v201 op_sel_hi:[0,0,0]
	v_mfma_scale_f32_16x16x128_f8f6f4 v[124:127], v[24:31], v[36:43], v[124:127], v201, v201 op_sel_hi:[0,0,0]
	v_mfma_scale_f32_16x16x128_f8f6f4 v[120:123], v[16:23], v[44:51], v[120:123], v201, v201 op_sel_hi:[0,0,0]
	v_mfma_scale_f32_16x16x128_f8f6f4 v[116:119], v[24:31], v[44:51], v[116:119], v201, v201 op_sel_hi:[0,0,0]
	v_mfma_scale_f32_16x16x128_f8f6f4 v[112:115], v[16:23], v[52:59], v[112:115], v201, v201 op_sel_hi:[0,0,0]
	v_mfma_scale_f32_16x16x128_f8f6f4 v[108:111], v[24:31], v[52:59], v[108:111], v201, v201 op_sel_hi:[0,0,0]
	v_mfma_scale_f32_16x16x128_f8f6f4 v[104:107], v[16:23], v[228:235], v[104:107], v201, v201 op_sel_hi:[0,0,0]
	v_mfma_scale_f32_16x16x128_f8f6f4 v[100:103], v[24:31], v[228:235], v[100:103], v201, v201 op_sel_hi:[0,0,0]
	s_setprio 0
	s_setprio 1
	v_mfma_scale_f32_16x16x128_f8f6f4 v[96:99], v[8:15], v[36:43], v[96:99], v201, v201 op_sel_hi:[0,0,0]
	v_mfma_scale_f32_16x16x128_f8f6f4 v[92:95], v[0:7], v[36:43], v[92:95], v201, v201 op_sel_hi:[0,0,0]
	v_mfma_scale_f32_16x16x128_f8f6f4 v[88:91], v[8:15], v[44:51], v[88:91], v201, v201 op_sel_hi:[0,0,0]
	v_mfma_scale_f32_16x16x128_f8f6f4 v[84:87], v[0:7], v[44:51], v[84:87], v201, v201 op_sel_hi:[0,0,0]
	v_mfma_scale_f32_16x16x128_f8f6f4 v[80:83], v[8:15], v[52:59], v[80:83], v201, v201 op_sel_hi:[0,0,0]
	v_mfma_scale_f32_16x16x128_f8f6f4 v[76:79], v[0:7], v[52:59], v[76:79], v201, v201 op_sel_hi:[0,0,0]
	v_mfma_scale_f32_16x16x128_f8f6f4 v[72:75], v[8:15], v[228:235], v[72:75], v201, v201 op_sel_hi:[0,0,0]
	v_mfma_scale_f32_16x16x128_f8f6f4 v[68:71], v[0:7], v[228:235], v[68:71], v201, v201 op_sel_hi:[0,0,0]
	s_setprio 0
	s_barrier
	ds_read_b128 v[24:27], v205 offset:0x8000
	ds_read_b128 v[28:31], v205 offset:0x8400
	ds_read_b128 v[16:19], v205 offset:0x8800
	ds_read_b128 v[20:23], v205 offset:0x8c00
	ds_read_b128 v[36:39], v204 offset:0x8000
	ds_read_b128 v[40:43], v204 offset:0x8400
	ds_read_b128 v[44:47], v204 offset:0x8800
	ds_read_b128 v[48:51], v204 offset:0x8c00
	ds_read_b128 v[52:55], v204 offset:0x9000
	ds_read_b128 v[56:59], v204 offset:0x9400
	ds_read_b128 v[228:231], v204 offset:0x9800
	ds_read_b128 v[232:235], v204 offset:0x9c00
	ds_read_b128 v[8:11], v205 offset:0xc000
	ds_read_b128 v[12:15], v205 offset:0xc400
	ds_read_b128 v[0:3], v205 offset:0xc800
	ds_read_b128 v[4:7], v205 offset:0xcc00
	s_mov_b32 m0, s44
	v_cndmask_b32_e32 v62, v216, v34, vcc
	buffer_load_dwordx4 v62, s[4:7], s66 offen lds
	v_cndmask_b32_e32 v62, v215, v35, vcc
	s_mov_b32 m0, s45
	s_nop 0
	buffer_load_dwordx4 v62, s[4:7], s66 offen lds
	s_waitcnt vmcnt(8)
	s_waitcnt lgkmcnt(4)
	s_barrier
	s_setprio 1
	v_mfma_scale_f32_16x16x128_f8f6f4 v[192:195], v[24:31], v[36:43], v[192:195], v201, v201 op_sel_hi:[0,0,0]
	v_mfma_scale_f32_16x16x128_f8f6f4 v[188:191], v[16:23], v[36:43], v[188:191], v201, v201 op_sel_hi:[0,0,0]
	v_mfma_scale_f32_16x16x128_f8f6f4 v[184:187], v[24:31], v[44:51], v[184:187], v201, v201 op_sel_hi:[0,0,0]
	v_mfma_scale_f32_16x16x128_f8f6f4 v[180:183], v[16:23], v[44:51], v[180:183], v201, v201 op_sel_hi:[0,0,0]
	v_mfma_scale_f32_16x16x128_f8f6f4 v[176:179], v[24:31], v[52:59], v[176:179], v201, v201 op_sel_hi:[0,0,0]
	v_mfma_scale_f32_16x16x128_f8f6f4 v[172:175], v[16:23], v[52:59], v[172:175], v201, v201 op_sel_hi:[0,0,0]
	v_mfma_scale_f32_16x16x128_f8f6f4 v[168:171], v[24:31], v[228:235], v[168:171], v201, v201 op_sel_hi:[0,0,0]
	v_mfma_scale_f32_16x16x128_f8f6f4 v[164:167], v[16:23], v[228:235], v[164:167], v201, v201 op_sel_hi:[0,0,0]
	s_setprio 0
	s_setprio 1
	s_waitcnt lgkmcnt(2)
	v_mfma_scale_f32_16x16x128_f8f6f4 v[160:163], v[8:15], v[36:43], v[160:163], v201, v201 op_sel_hi:[0,0,0]
	s_waitcnt lgkmcnt(0)
	v_mfma_scale_f32_16x16x128_f8f6f4 v[156:159], v[0:7], v[36:43], v[156:159], v201, v201 op_sel_hi:[0,0,0]
	v_mfma_scale_f32_16x16x128_f8f6f4 v[152:155], v[8:15], v[44:51], v[152:155], v201, v201 op_sel_hi:[0,0,0]
	v_mfma_scale_f32_16x16x128_f8f6f4 v[148:151], v[0:7], v[44:51], v[148:151], v201, v201 op_sel_hi:[0,0,0]
	v_mfma_scale_f32_16x16x128_f8f6f4 v[144:147], v[8:15], v[52:59], v[144:147], v201, v201 op_sel_hi:[0,0,0]
	v_mfma_scale_f32_16x16x128_f8f6f4 v[140:143], v[0:7], v[52:59], v[140:143], v201, v201 op_sel_hi:[0,0,0]
	v_mfma_scale_f32_16x16x128_f8f6f4 v[136:139], v[8:15], v[228:235], v[136:139], v201, v201 op_sel_hi:[0,0,0]
	v_mfma_scale_f32_16x16x128_f8f6f4 v[132:135], v[0:7], v[228:235], v[132:135], v201, v201 op_sel_hi:[0,0,0]
	s_setprio 0
	s_barrier
	ds_read_b128 v[36:39], v204 offset:0xc000
	ds_read_b128 v[40:43], v204 offset:0xc400
	ds_read_b128 v[44:47], v204 offset:0xc800
	ds_read_b128 v[48:51], v204 offset:0xcc00
	ds_read_b128 v[52:55], v204 offset:0xd000
	ds_read_b128 v[56:59], v204 offset:0xd400
	ds_read_b128 v[228:231], v204 offset:0xd800
	ds_read_b128 v[232:235], v204 offset:0xdc00
	s_mov_b32 m0, s48
	s_add_i32 s66, s61, 0x80
	buffer_load_dwordx4 v203, s[8:11], s66 offen lds
	s_add_i32 s66, s61, 0x80080
	s_mov_b32 m0, s49
	s_nop 0
	buffer_load_dwordx4 v203, s[8:11], s66 offen lds
	s_add_i32 s66, s61, 0x8080
	s_mov_b32 m0, s62
	s_add_i32 s61, s61, 0x88080
	buffer_load_dwordx4 v203, s[8:11], s66 offen lds
	s_mov_b32 m0, s63
	s_nop 0
	buffer_load_dwordx4 v203, s[8:11], s61 offen lds
	s_mov_b32 m0, s50
	s_nop 0
	buffer_load_dwordx4 v60, s[4:7], s60 offen lds
	s_mov_b32 m0, s51
	s_nop 0
	buffer_load_dwordx4 v61, s[4:7], s60 offen lds
	s_waitcnt vmcnt(8)
	s_waitcnt lgkmcnt(0)
	s_barrier
	s_setprio 1
	v_mfma_scale_f32_16x16x128_f8f6f4 v[128:131], v[24:31], v[36:43], v[128:131], v201, v201 op_sel_hi:[0,0,0]
	v_mfma_scale_f32_16x16x128_f8f6f4 v[124:127], v[16:23], v[36:43], v[124:127], v201, v201 op_sel_hi:[0,0,0]
	v_mfma_scale_f32_16x16x128_f8f6f4 v[120:123], v[24:31], v[44:51], v[120:123], v201, v201 op_sel_hi:[0,0,0]
	v_mfma_scale_f32_16x16x128_f8f6f4 v[116:119], v[16:23], v[44:51], v[116:119], v201, v201 op_sel_hi:[0,0,0]
	v_mfma_scale_f32_16x16x128_f8f6f4 v[112:115], v[24:31], v[52:59], v[112:115], v201, v201 op_sel_hi:[0,0,0]
	v_mfma_scale_f32_16x16x128_f8f6f4 v[108:111], v[16:23], v[52:59], v[108:111], v201, v201 op_sel_hi:[0,0,0]
	v_mfma_scale_f32_16x16x128_f8f6f4 v[104:107], v[24:31], v[228:235], v[104:107], v201, v201 op_sel_hi:[0,0,0]
	v_mfma_scale_f32_16x16x128_f8f6f4 v[100:103], v[16:23], v[228:235], v[100:103], v201, v201 op_sel_hi:[0,0,0]
	s_setprio 0
	s_setprio 1
	v_mfma_scale_f32_16x16x128_f8f6f4 v[96:99], v[8:15], v[36:43], v[96:99], v201, v201 op_sel_hi:[0,0,0]
	v_mfma_scale_f32_16x16x128_f8f6f4 v[92:95], v[0:7], v[36:43], v[92:95], v201, v201 op_sel_hi:[0,0,0]
	v_mfma_scale_f32_16x16x128_f8f6f4 v[88:91], v[8:15], v[44:51], v[88:91], v201, v201 op_sel_hi:[0,0,0]
	v_mfma_scale_f32_16x16x128_f8f6f4 v[84:87], v[0:7], v[44:51], v[84:87], v201, v201 op_sel_hi:[0,0,0]
	v_mfma_scale_f32_16x16x128_f8f6f4 v[80:83], v[8:15], v[52:59], v[80:83], v201, v201 op_sel_hi:[0,0,0]
	v_mfma_scale_f32_16x16x128_f8f6f4 v[76:79], v[0:7], v[52:59], v[76:79], v201, v201 op_sel_hi:[0,0,0]
	v_mfma_scale_f32_16x16x128_f8f6f4 v[72:75], v[8:15], v[228:235], v[72:75], v201, v201 op_sel_hi:[0,0,0]
	v_mfma_scale_f32_16x16x128_f8f6f4 v[68:71], v[0:7], v[228:235], v[68:71], v201, v201 op_sel_hi:[0,0,0]
	s_setprio 0
	s_add_i32 s33, s33, 2
	s_addk_i32 s28, 0x100
	s_addk_i32 s29, 0x100
	s_cmp_gt_u32 s33, 29
	s_cbranch_scc1 .Lp8_exit
	s_add_i32 s66, s28, 0x80
	s_cmp_eq_u32 s33, 28
	s_cselect_b64 vcc, -1, 0
	s_branch .LBB0_1229
.Lp8_exit:
	s_barrier
	s_and_b64 vcc, exec, s[18:19]
	s_cbranch_vccz .LBB0_1232
	s_barrier
